# DSA unit preambles: batch the 8 first-tile K index reads (nsel==256) and overlap the indexer head-weight load with the query fragment loads
# speedup vs baseline: 1.0072x; 1.0029x over previous
.LBB0_541:
	s_andn2_b64 vcc, exec, s[6:7]
	s_cbranch_vccnz .LBB0_890
	s_sub_i32 s5, s78, s1
	v_readlane_b32 s6, v255, 48
	s_add_i32 s5, s6, s5
	s_ashr_i32 s6, s5, 31
	s_lshr_b32 s6, s6, 25
	s_lshl_b32 s17, s5, 4
	s_add_i32 s6, s5, s6
	s_bfe_i32 s5, s5, 0x1001b
	s_lshr_b32 s5, s5, 21
	s_add_i32 s5, s17, s5
	s_and_b32 s5, s5, 0xfffff800
	s_sub_i32 s20, s17, s5
	s_ashr_i32 s42, s6, 7
	s_and_b32 s12, s20, 0xffffffc0
	s_add_i32 s18, s12, 64
	s_ashr_i32 s43, s42, 31
	v_and_b32_e32 v71, 15, v146
	v_lshrrev_b32_e32 v49, 4, v245
	s_cmpk_lt_i32 s12, 0x100
	v_lshlrev_b32_e32 v74, 2, v71
	s_brev_b32 s30, 1
	s_cbranch_scc1 .LBB0_558
	s_lshr_b32 s19, s18, 4
	s_cmp_ge_i32 s4, s19
	s_cbranch_scc1 .LBB0_558
	v_or_b32_e32 v2, s17, v71
	v_mov_b64_e32 v[0:1], s[88:89]
	v_mad_i64_i32 v[0:1], s[6:7], v2, s10, v[0:1]
	v_add_co_u32_e32 v2, vcc, 0x2000, v0
	s_mov_b64 s[6:7], 0x1500
	s_nop 0
	v_addc_co_u32_e32 v3, vcc, 0, v1, vcc
	global_load_dwordx2 v[192:193], v[2:3], off offset:896
	s_lshr_b32 s21, s18, 5
	v_cvt_f32_u32_e32 v32, s21
	s_sub_i32 s24, 0, s21
	v_lshlrev_b32_e32 v34, 2, v49
	v_mov_b32_e32 v33, v48
	v_rcp_iflag_f32_e32 v32, v32
	v_lshl_add_u32 v75, v71, 13, 0
	v_mul_f32_e32 v32, 0x4f7ffffe, v32
	v_cvt_u32_f32_e32 v32, v32
	v_lshlrev_b32_e32 v2, 4, v49
	v_mov_b32_e32 v3, v48
	v_lshl_add_u64 v[28:29], v[0:1], 0, v[2:3]
	v_lshl_add_u64 v[24:25], v[28:29], 0, s[6:7]
	global_load_dwordx4 v[0:3], v[24:25], off offset:448
	global_load_dwordx4 v[4:7], v[24:25], off offset:384
	global_load_dwordx4 v[8:11], v[24:25], off offset:320
	global_load_dwordx4 v[12:15], v[24:25], off offset:256
	global_load_dwordx4 v[16:19], v[24:25], off offset:192
	global_load_dwordx4 v[20:23], v[24:25], off offset:128
	s_nop 0
	global_load_dwordx4 v[24:27], v[24:25], off offset:64
	v_add_co_u32_e32 v28, vcc, s16, v28
	v_readfirstlane_b32 s5, v32
	s_nop 0
	v_addc_co_u32_e32 v29, vcc, 0, v29, vcc
	global_load_dwordx4 v[28:31], v[28:29], off offset:1280
	s_waitcnt vmcnt(8)
	v_and_b32_e32 v195, 0xffff0000, v192
	v_lshlrev_b32_e32 v194, 16, v192
	v_pk_mul_f32 v[66:67], v[194:195], 0.5 op_sel_hi:[1,0]
	v_and_b32_e32 v195, 0xffff0000, v193
	v_lshlrev_b32_e32 v194, 16, v193
	v_pk_mul_f32 v[68:69], v[194:195], 0.5 op_sel_hi:[1,0]
	s_mul_i32 s6, s24, s5
	s_mul_hi_u32 s6, s5, s6
	s_add_i32 s5, s5, s6
	s_mul_hi_u32 s5, s5, -1
	s_mul_i32 s6, s5, s21
	s_not_b32 s6, s6
	s_add_i32 s7, s5, 1
	s_sub_i32 s8, s6, s21
	s_cmp_ge_u32 s6, s21
	s_cselect_b32 s5, s7, s5
	s_cselect_b32 s6, s8, s6
	s_add_i32 s7, s5, 1
	s_cmp_ge_u32 s6, s21
	s_cselect_b32 s5, s7, s5
	s_add_i32 s25, s5, 1
	s_lshl_b32 s28, s4, 4
	s_lshl_b32 s5, s4, 9
	v_lshlrev_b32_e32 v32, 7, v49
	v_or3_b32 v70, s5, v32, v74
	s_add_i32 s5, s28, 0x180
	v_or_b32_e32 v77, s5, v34
	s_ashr_i32 s5, s4, 31
	s_lshl_b64 s[6:7], s[42:43], 18
	s_sub_i32 s26, 0xffffffc1, s12
	s_lshl_b64 s[8:9], s[4:5], 11
	s_add_u32 s5, s6, s8
	s_addc_u32 s7, s7, s9
	v_readlane_b32 s6, v255, 56
	s_add_u32 s6, s6, s5
	v_readlane_b32 s5, v255, 57
	v_or_b32_e32 v76, s28, v34
	v_lshlrev_b32_e32 v32, 4, v245
	s_addc_u32 s7, s5, s7
	s_add_i32 s5, s28, 0x100
	s_addk_i32 s28, 0x80
	v_lshl_add_u64 v[72:73], s[6:7], 0, v[32:33]
	v_or_b32_e32 v78, s5, v34
	v_or_b32_e32 v79, s28, v34
	s_mov_b32 s5, s4
	s_branch .LBB0_546

.LBB0_773:
	s_or_b64 exec, exec, s[6:7]
	s_lshl_b64 s[6:7], s[42:43], 19
	s_add_u32 s50, s66, s6
	s_addc_u32 s51, s67, s7
	s_lshl_b32 s6, s5, 2
	s_add_i32 s6, s6, 0
	s_add_i32 s6, s6, 0x22000
	v_mov_b32_e32 v0, s6
	s_waitcnt lgkmcnt(0)
	ds_read_b32 v0, v0
	s_lshl_b32 s7, s4, 10
	s_add_i32 s7, s7, 0
	v_lshrrev_b32_e32 v147, 2, v245
	v_and_b32_e32 v44, 3, v146
	s_add_i32 s7, s7, 0x20000
	s_waitcnt lgkmcnt(0)
	v_cmp_gt_i32_e32 vcc, 1, v0
	v_readlane_b32 s24, v255, 30
	v_readfirstlane_b32 s6, v0
	v_lshlrev_b32_e32 v246, 4, v44
	s_and_b64 vcc, exec, vcc
	v_lshl_add_u32 v45, v147, 1, s7
	v_readlane_b32 s25, v255, 31
	v_readlane_b32 s26, v255, 18
	s_cmpk_eq_i32 s6, 0x100
	s_cbranch_scc1 .Lmy_kpre
	s_cbranch_vccnz .LBB0_775
	ds_read_u16 v0, v45
	s_waitcnt lgkmcnt(0)
	v_lshl_or_b32 v4, v0, 8, v246
	global_load_dwordx4 v[0:3], v4, s[50:51]
	s_nop 0
	global_load_dwordx4 v[4:7], v4, s[50:51] offset:64

.Lmy_kpre:
	ds_read_u16 v0, v45
	ds_read_u16 v8, v45 offset:32
	ds_read_u16 v16, v45 offset:64
	ds_read_u16 v24, v45 offset:96
	ds_read_u16 v32, v45 offset:128
	ds_read_u16 v40, v45 offset:160
	ds_read_u16 v54, v45 offset:192
	ds_read_u16 v62, v45 offset:224
	s_waitcnt lgkmcnt(0)
	v_lshl_or_b32 v4, v0, 8, v246
	global_load_dwordx4 v[0:3], v4, s[50:51]
	global_load_dwordx4 v[4:7], v4, s[50:51] offset:64
	v_lshl_or_b32 v12, v8, 8, v246
	global_load_dwordx4 v[8:11], v12, s[50:51]
	global_load_dwordx4 v[12:15], v12, s[50:51] offset:64
	v_lshl_or_b32 v20, v16, 8, v246
	global_load_dwordx4 v[16:19], v20, s[50:51]
	global_load_dwordx4 v[20:23], v20, s[50:51] offset:64
	v_lshl_or_b32 v28, v24, 8, v246
	global_load_dwordx4 v[24:27], v28, s[50:51]
	global_load_dwordx4 v[28:31], v28, s[50:51] offset:64
	v_lshl_or_b32 v36, v32, 8, v246
	global_load_dwordx4 v[32:35], v36, s[50:51]
	global_load_dwordx4 v[36:39], v36, s[50:51] offset:64
	v_lshl_or_b32 v50, v40, 8, v246
	global_load_dwordx4 v[40:43], v50, s[50:51]
	global_load_dwordx4 v[50:53], v50, s[50:51] offset:64
	v_lshl_or_b32 v58, v54, 8, v246
	global_load_dwordx4 v[54:57], v58, s[50:51]
	global_load_dwordx4 v[58:61], v58, s[50:51] offset:64
	v_lshl_or_b32 v66, v62, 8, v246
	global_load_dwordx4 v[62:65], v66, s[50:51]
	global_load_dwordx4 v[66:69], v66, s[50:51] offset:64
	s_branch .LBB0_783
